# vaccH LDS half: the token-block head waits with vmcnt(2) (both H stores of the previous block may stay in flight; stores issue unconditionally)
# speedup vs baseline: 1.0083x; 1.0083x over previous
; #define VL_LOAD(wr, C) do { _Pragma("unroll") for (int i = 0; i < 16; ++i) wr[i] = wp[(size_t)((C) * 16 + i) * MROWS]; } while (0)
; #define VL_LOAD(wr, C) do { _Pragma("unroll") for (int i = 0; i < 16; ++i) wr[i] = wp[(size_t)((C) * 16 + i) * MROWS]; } while (0)
; template <bool RUN_L = true, bool RUN_G = true, bool DRY = false>
; __device__ __forceinline__ void phase_vaccH(unsigned char* ws, LAS unsigned char* lds, int layer, int G) {
;     ...
;             for (int tb = wid; tb < NTB; tb += 4) {
;                 const int tok = tb * 64 + lane; const bool valid = tok < MROWS; const int tokc = valid ? tok : MROWS - 1;
;                 const unsigned* wp = WLT + tokc;
;                 f32x4* hp = (f32x4*)(H + (size_t)tokc * D + cg * 8); const f32x4 h0 = hp[0], h1 = hp[1];
;                 float accf[8];
; #pragma unroll
;                 for (int j = 0; j < 8; ++j) accf[j] = 0.f;
;                 unsigned wa[16], wb[16];
;                 VL_LOAD(wa, 0);
; #pragma unroll 1
;                 for (int c = 0; c < 8; c += 2) {
;                     VL_LOAD(wb, c + 1);
;                     __builtin_amdgcn_sched_barrier(0);
;                     VL_CHUNK(wa);
.LBB0_1241:
	s_waitcnt vmcnt(2)
	v_lshl_or_b32 v2, s29, 6, v1
	s_movk_i32 s6, 0x2010
	v_cmp_gt_i32_e64 s[6:7], s6, v2
	v_mov_b32_e32 v28, 0
	s_mov_b32 s46, 32
	v_cndmask_b32_e64 v12, v171, v2, s[6:7]
	v_ashrrev_i32_e32 v13, 31, v12
	v_lshlrev_b64 v[14:15], 2, v[12:13]
	v_mov_b32_e32 v238, v14
	v_lshlrev_b64 v[2:3], 14, v[12:13]
	v_lshl_add_u64 v[12:13], s[16:17], 0, v[14:15]
	v_lshl_add_u64 v[10:11], s[30:31], 0, v[2:3]
	global_load_dwordx4 v[2:5], v[10:11], off offset:16
	global_load_dwordx4 v[6:9], v[10:11], off
	global_load_dword v36, v238, s[16:17]
	s_add_u32 s78, s16, s62
	s_addc_u32 s79, s17, 0
	global_load_dword v37, v238, s[78:79] offset:64
	v_lshl_add_u64 v[14:15], s[18:19], 0, v[14:15]
	s_mov_b64 s[76:77], s[18:19]
	s_add_u32 s78, s16, s56
	s_addc_u32 s79, s17, 0
	global_load_dword v38, v238, s[78:79] offset:128
	s_mov_b32 s47, -2
	s_add_u32 s78, s16, s57
	s_addc_u32 s79, s17, 0
	global_load_dword v39, v238, s[78:79] offset:192
	v_mov_b32_e32 v29, v28
	s_add_u32 s78, s16, s64
	s_addc_u32 s79, s17, 0
	global_load_dword v40, v238, s[78:79] offset:256
	v_mov_b32_e32 v34, v28
	s_add_u32 s78, s16, s65
	s_addc_u32 s79, s17, 0
	global_load_dword v41, v238, s[78:79] offset:320
	v_mov_b32_e32 v35, v28
	s_add_u32 s78, s16, s66
	s_addc_u32 s79, s17, 0
	global_load_dword v42, v238, s[78:79] offset:384
	v_mov_b32_e32 v22, v28
	s_add_u32 s78, s16, s67
	s_addc_u32 s79, s17, 0
	global_load_dword v44, v238, s[78:79] offset:448
	v_mov_b32_e32 v23, v28
	s_add_u32 s78, s16, s68
	s_addc_u32 s79, s17, 0
	global_load_dword v43, v238, s[78:79] offset:512
	v_mov_b32_e32 v20, v28
	s_add_u32 s78, s16, s69
	s_addc_u32 s79, s17, 0
	global_load_dword v45, v238, s[78:79] offset:576
	v_mov_b32_e32 v21, v28
	s_add_u32 s78, s16, s70
	s_addc_u32 s79, s17, 0
	global_load_dword v46, v238, s[78:79] offset:640
	s_add_u32 s78, s16, s71
	s_addc_u32 s79, s17, 0
	global_load_dword v47, v238, s[78:79] offset:704
	s_add_u32 s78, s16, s72
	s_addc_u32 s79, s17, 0
	global_load_dword v48, v238, s[78:79] offset:768
	s_add_u32 s78, s16, 0x68000
	s_addc_u32 s79, s17, 0
	global_load_dword v49, v238, s[78:79] offset:832
	s_add_u32 s78, s16, 0x70000
	s_addc_u32 s79, s17, 0
	global_load_dword v50, v238, s[78:79] offset:896
	s_add_u32 s78, s16, 0x78000
	s_addc_u32 s79, s17, 0
	global_load_dword v51, v238, s[78:79] offset:960
.LBB0_1242:
	global_load_dword v24, v238, s[76:77]
	s_add_u32 s78, s76, s62
	s_addc_u32 s79, s77, 0
	global_load_dword v31, v238, s[78:79] offset:64
	v_mov_b32_e32 v19, v29
	s_add_u32 s78, s76, s56
	s_addc_u32 s79, s77, 0
	global_load_dword v30, v238, s[78:79] offset:128
	v_mov_b32_e32 v18, v28
	s_add_u32 s78, s76, s57
	s_addc_u32 s79, s77, 0
	global_load_dword v29, v238, s[78:79] offset:192
	v_mov_b32_e32 v17, v35
	s_add_u32 s78, s76, s64
	s_addc_u32 s79, s77, 0
	global_load_dword v28, v238, s[78:79] offset:256
	v_mov_b32_e32 v16, v34
	s_add_u32 s78, s76, s65
	s_addc_u32 s79, s77, 0
	global_load_dword v27, v238, s[78:79] offset:320
	s_add_u32 s78, s76, s66
	s_addc_u32 s79, s77, 0
	global_load_dword v26, v238, s[78:79] offset:384
	s_add_u32 s78, s76, s67
	s_addc_u32 s79, s77, 0
	global_load_dword v25, v238, s[78:79] offset:448
	s_add_u32 s78, s76, s68
	s_addc_u32 s79, s77, 0
	global_load_dword v54, v238, s[78:79] offset:512
	s_add_u32 s78, s76, s69
	s_addc_u32 s79, s77, 0
	global_load_dword v53, v238, s[78:79] offset:576
	s_add_u32 s78, s76, s70
	s_addc_u32 s79, s77, 0
	global_load_dword v52, v238, s[78:79] offset:640
	s_add_u32 s78, s76, s71
	s_addc_u32 s79, s77, 0
	global_load_dword v35, v238, s[78:79] offset:704
	s_add_u32 s78, s76, s72
	s_addc_u32 s79, s77, 0
	global_load_dword v34, v238, s[78:79] offset:768
	s_add_u32 s78, s76, s73
	s_addc_u32 s79, s77, 0
	global_load_dword v33, v238, s[78:79] offset:832
	s_add_u32 s78, s76, s74
	s_addc_u32 s79, s77, 0
	global_load_dword v32, v238, s[78:79] offset:896
	s_add_u32 s78, s76, s75
	s_addc_u32 s79, s77, 0
	global_load_dword v55, v238, s[78:79] offset:960
	s_waitcnt vmcnt(30)
	v_bfe_u32 v57, v37, 16, 16
	v_lshl_add_u32 v58, v57, 3, 0
	s_waitcnt vmcnt(29)
	v_bfe_u32 v57, v38, 16, 16
	v_bfe_u32 v56, v36, 16, 16
	v_lshl_add_u32 v60, v57, 3, 0
	s_waitcnt vmcnt(28)
	v_bfe_u32 v57, v39, 16, 16
	v_lshl_add_u32 v56, v56, 3, 0
	v_lshl_add_u32 v62, v57, 3, 0
	ds_read_b64 v[56:57], v56
	ds_read_b64 v[58:59], v58
	ds_read_b64 v[60:61], v60
	ds_read_b64 v[62:63], v62
	v_perm_b32 v36, v36, v36, s63
	s_waitcnt lgkmcnt(3)
	v_perm_b32 v88, 0, v56, v169
	v_perm_b32 v56, 0, v56, v170
	v_perm_b32 v89, 0, v57, v169
	v_perm_b32 v57, 0, v57, v170
	v_pk_fma_f16 v88, v36, v88, 0
	v_pk_fma_f16 v56, v36, v56, 0
	v_pk_fma_f16 v89, v36, v89, 0
	v_pk_fma_f16 v36, v36, v57, 0
	v_perm_b32 v37, v37, v37, s63
	s_waitcnt lgkmcnt(2)
	v_perm_b32 v57, 0, v58, v169
	v_perm_b32 v58, 0, v58, v170
	v_pk_fma_f16 v56, v37, v58, v56
	v_perm_b32 v58, 0, v59, v169
	v_perm_b32 v59, 0, v59, v170
	v_pk_fma_f16 v57, v37, v57, v88
	v_pk_fma_f16 v58, v37, v58, v89
	v_pk_fma_f16 v36, v37, v59, v36
	v_perm_b32 v37, v38, v38, s63
	s_waitcnt lgkmcnt(1)
	v_perm_b32 v38, 0, v60, v169
	v_pk_fma_f16 v38, v37, v38, v57
	v_perm_b32 v57, 0, v60, v170
	s_waitcnt vmcnt(26)
	v_bfe_u32 v65, v41, 16, 16
	v_pk_fma_f16 v56, v37, v57, v56
	v_perm_b32 v57, 0, v61, v169
	v_lshl_add_u32 v66, v65, 3, 0
	s_waitcnt vmcnt(25)
	v_bfe_u32 v65, v42, 16, 16
	v_pk_fma_f16 v57, v37, v57, v58
	v_perm_b32 v58, 0, v61, v170
	v_bfe_u32 v64, v40, 16, 16
	v_lshl_add_u32 v68, v65, 3, 0
	s_waitcnt vmcnt(24)
	v_bfe_u32 v65, v44, 16, 16
	v_pk_fma_f16 v36, v37, v58, v36
	v_perm_b32 v37, v39, v39, s63
	s_waitcnt lgkmcnt(0)
; #define VL_LOAD(wr, C) do { _Pragma("unroll") for (int i = 0; i < 16; ++i) wr[i] = wp[(size_t)((C) * 16 + i) * MROWS]; } while (0)
; #define VL_LOAD(wr, C) do { _Pragma("unroll") for (int i = 0; i < 16; ++i) wr[i] = wp[(size_t)((C) * 16 + i) * MROWS]; } while (0)
; template <bool RUN_L = true, bool RUN_G = true, bool DRY = false>
; __device__ __forceinline__ void phase_vaccH(unsigned char* ws, LAS unsigned char* lds, int layer, int G) {
;     ...
; #pragma unroll 1
;             for (int tb = wid; tb < NTB; tb += 4) {
;                 const int tok = tb * 64 + lane; const bool valid = tok < MROWS; const int tokc = valid ? tok : MROWS - 1;
;                 const unsigned* wp = WLT + tokc;
;                 f32x4* hp = (f32x4*)(H + (size_t)tokc * D + cg * 8); const f32x4 h0 = hp[0], h1 = hp[1];
;                 float accf[8];
; #pragma unroll
;                 for (int j = 0; j < 8; ++j) accf[j] = 0.f;
;                 unsigned wa[16], wb[16];
;                 VL_LOAD(wa, 0);
; #pragma unroll 1
;                 for (int c = 0; c < 8; c += 2) {
;                     VL_LOAD(wb, c + 1);
;                     __builtin_amdgcn_sched_barrier(0);
;                     VL_CHUNK(wa);
;                     __builtin_amdgcn_sched_barrier(0);
;                     VL_LOAD(wa, (c + 2) & 7);
	v_perm_b32 v39, 0, v62, v169
	v_lshl_add_u32 v64, v64, 3, 0
	v_lshl_add_u32 v70, v65, 3, 0
	v_pk_fma_f16 v38, v37, v39, v38
	v_perm_b32 v39, 0, v62, v170
	ds_read_b64 v[64:65], v64
	ds_read_b64 v[66:67], v66
	ds_read_b64 v[68:69], v68
	ds_read_b64 v[70:71], v70
	v_pk_fma_f16 v39, v37, v39, v56
	v_perm_b32 v56, 0, v63, v169
	v_pk_fma_f16 v56, v37, v56, v57
	v_perm_b32 v57, 0, v63, v170
	v_pk_fma_f16 v36, v37, v57, v36
	v_perm_b32 v37, v40, v40, s63
	s_waitcnt lgkmcnt(3)
	v_perm_b32 v40, 0, v64, v169
	v_pk_fma_f16 v38, v37, v40, v38
	v_perm_b32 v40, 0, v64, v170
	v_pk_fma_f16 v39, v37, v40, v39
	v_perm_b32 v40, 0, v65, v169
	v_pk_fma_f16 v40, v37, v40, v56
	v_perm_b32 v56, 0, v65, v170
	v_pk_fma_f16 v36, v37, v56, v36
	v_perm_b32 v37, v41, v41, s63
	s_waitcnt lgkmcnt(2)
	v_perm_b32 v41, 0, v66, v169
	v_pk_fma_f16 v38, v37, v41, v38
	v_perm_b32 v41, 0, v66, v170
	v_pk_fma_f16 v39, v37, v41, v39
	v_perm_b32 v41, 0, v67, v169
	v_pk_fma_f16 v40, v37, v41, v40
	v_perm_b32 v41, 0, v67, v170
	v_pk_fma_f16 v36, v37, v41, v36
	v_perm_b32 v37, v42, v42, s63
	s_waitcnt lgkmcnt(1)
	v_perm_b32 v41, 0, v68, v169
	v_pk_fma_f16 v38, v37, v41, v38
	v_perm_b32 v41, 0, v68, v170
	s_waitcnt vmcnt(22)
	v_bfe_u32 v73, v45, 16, 16
	v_pk_fma_f16 v39, v37, v41, v39
	v_perm_b32 v41, 0, v69, v169
	v_lshl_add_u32 v74, v73, 3, 0
	s_waitcnt vmcnt(21)
	v_bfe_u32 v73, v46, 16, 16
	v_pk_fma_f16 v40, v37, v41, v40
	v_perm_b32 v41, 0, v69, v170
	v_bfe_u32 v72, v43, 16, 16
	v_lshl_add_u32 v76, v73, 3, 0
	s_waitcnt vmcnt(20)
	v_bfe_u32 v73, v47, 16, 16
	v_pk_fma_f16 v36, v37, v41, v36
	v_perm_b32 v37, v44, v44, s63
	s_waitcnt lgkmcnt(0)
	v_perm_b32 v41, 0, v70, v169
	v_lshl_add_u32 v72, v72, 3, 0
	v_lshl_add_u32 v78, v73, 3, 0
	v_pk_fma_f16 v38, v37, v41, v38
	v_perm_b32 v41, 0, v70, v170
	ds_read_b64 v[72:73], v72
	ds_read_b64 v[74:75], v74
	ds_read_b64 v[76:77], v76
	ds_read_b64 v[78:79], v78
	v_pk_fma_f16 v39, v37, v41, v39
	v_perm_b32 v41, 0, v71, v169
	v_pk_fma_f16 v40, v37, v41, v40
	v_perm_b32 v41, 0, v71, v170
	v_pk_fma_f16 v36, v37, v41, v36
	v_perm_b32 v37, v43, v43, s63
	s_waitcnt lgkmcnt(3)
	v_perm_b32 v41, 0, v72, v169
	v_pk_fma_f16 v38, v37, v41, v38
	v_perm_b32 v41, 0, v72, v170
	v_pk_fma_f16 v39, v37, v41, v39
	v_perm_b32 v41, 0, v73, v169
	v_pk_fma_f16 v40, v37, v41, v40
	v_perm_b32 v41, 0, v73, v170
	v_pk_fma_f16 v36, v37, v41, v36
	v_perm_b32 v37, v45, v45, s63
	s_waitcnt lgkmcnt(2)
	v_perm_b32 v41, 0, v74, v169
	v_pk_fma_f16 v38, v37, v41, v38
	v_perm_b32 v41, 0, v74, v170
	v_pk_fma_f16 v39, v37, v41, v39
	v_perm_b32 v41, 0, v75, v169
	v_pk_fma_f16 v40, v37, v41, v40
	v_perm_b32 v41, 0, v75, v170
	v_pk_fma_f16 v36, v37, v41, v36
	v_perm_b32 v37, v46, v46, s63
	s_waitcnt lgkmcnt(1)
	v_perm_b32 v41, 0, v76, v169
	v_pk_fma_f16 v38, v37, v41, v38
	v_perm_b32 v41, 0, v76, v170
	s_waitcnt vmcnt(18)
	v_bfe_u32 v81, v49, 16, 16
	v_pk_fma_f16 v39, v37, v41, v39
	v_perm_b32 v41, 0, v77, v169
	v_lshl_add_u32 v82, v81, 3, 0
	s_waitcnt vmcnt(17)
	v_bfe_u32 v81, v50, 16, 16
	v_pk_fma_f16 v40, v37, v41, v40
	v_perm_b32 v41, 0, v77, v170
	v_bfe_u32 v80, v48, 16, 16
	v_lshl_add_u32 v84, v81, 3, 0
	s_waitcnt vmcnt(16)
	v_bfe_u32 v81, v51, 16, 16
	v_pk_fma_f16 v36, v37, v41, v36
	v_perm_b32 v37, v47, v47, s63
	s_waitcnt lgkmcnt(0)
	v_perm_b32 v41, 0, v78, v169
	v_lshl_add_u32 v80, v80, 3, 0
	v_lshl_add_u32 v86, v81, 3, 0
	v_pk_fma_f16 v38, v37, v41, v38
	v_perm_b32 v41, 0, v78, v170
	ds_read_b64 v[80:81], v80
	ds_read_b64 v[82:83], v82
	ds_read_b64 v[84:85], v84
	ds_read_b64 v[86:87], v86
	v_pk_fma_f16 v39, v37, v41, v39
	v_perm_b32 v41, 0, v79, v169
	v_pk_fma_f16 v40, v37, v41, v40
	v_perm_b32 v41, 0, v79, v170
	v_pk_fma_f16 v36, v37, v41, v36
	v_perm_b32 v37, v48, v48, s63
	s_waitcnt lgkmcnt(3)
	v_perm_b32 v41, 0, v80, v169
	v_pk_fma_f16 v38, v37, v41, v38
	v_perm_b32 v41, 0, v80, v170
	v_pk_fma_f16 v39, v37, v41, v39
	v_perm_b32 v41, 0, v81, v169
	v_pk_fma_f16 v40, v37, v41, v40
	v_perm_b32 v41, 0, v81, v170
	v_pk_fma_f16 v36, v37, v41, v36
	v_perm_b32 v37, v49, v49, s63
	s_waitcnt lgkmcnt(2)
	v_perm_b32 v41, 0, v82, v169
	v_pk_fma_f16 v38, v37, v41, v38
	v_perm_b32 v41, 0, v82, v170
	v_pk_fma_f16 v39, v37, v41, v39
	v_perm_b32 v41, 0, v83, v169
	v_pk_fma_f16 v40, v37, v41, v40
	v_perm_b32 v41, 0, v83, v170
	v_pk_fma_f16 v36, v37, v41, v36
	v_perm_b32 v37, v50, v50, s63
	s_waitcnt lgkmcnt(1)
	v_perm_b32 v41, 0, v84, v169
	v_pk_fma_f16 v38, v37, v41, v38
	v_perm_b32 v41, 0, v84, v170
	v_pk_fma_f16 v39, v37, v41, v39
	v_perm_b32 v41, 0, v85, v169
	v_pk_fma_f16 v40, v37, v41, v40
	v_perm_b32 v41, 0, v85, v170
	v_pk_fma_f16 v36, v37, v41, v36
	v_perm_b32 v37, v51, v51, s63
	s_waitcnt lgkmcnt(0)
	v_perm_b32 v41, 0, v86, v169
	v_pk_fma_f16 v58, v37, v41, v38
	v_perm_b32 v38, 0, v86, v170
	v_pk_fma_f16 v59, v37, v38, v39
	v_perm_b32 v38, 0, v87, v169
	v_pk_fma_f16 v60, v37, v38, v40
	v_perm_b32 v38, 0, v87, v170
	v_pk_fma_f16 v61, v37, v38, v36
	s_and_b32 s8, s46, 0x60
	s_mul_i32 s8, s8, 0x8040
	s_add_u32 s98, s16, s8
	s_addc_u32 s99, s17, 0
	global_load_dword v36, v238, s[98:99]
	s_add_u32 s78, s98, s62
	s_addc_u32 s79, s99, 0
	global_load_dword v37, v238, s[78:79] offset:64
	s_add_u32 s78, s98, s56
	s_addc_u32 s79, s99, 0
	global_load_dword v38, v238, s[78:79] offset:128
	s_add_u32 s78, s98, s57
	s_addc_u32 s79, s99, 0
	global_load_dword v39, v238, s[78:79] offset:192
	s_add_u32 s78, s98, s64
	s_addc_u32 s79, s99, 0
	global_load_dword v40, v238, s[78:79] offset:256
	s_add_u32 s78, s98, s65
	s_addc_u32 s79, s99, 0
	global_load_dword v41, v238, s[78:79] offset:320
	s_add_u32 s78, s98, s66
	s_addc_u32 s79, s99, 0
	global_load_dword v42, v238, s[78:79] offset:384
	s_add_u32 s78, s98, s67
	s_addc_u32 s79, s99, 0
	global_load_dword v44, v238, s[78:79] offset:448
	s_add_u32 s78, s98, s68
	s_addc_u32 s79, s99, 0
	global_load_dword v43, v238, s[78:79] offset:512
	s_add_u32 s78, s98, s69
	s_addc_u32 s79, s99, 0
	global_load_dword v45, v238, s[78:79] offset:576
	s_add_u32 s78, s98, s70
	s_addc_u32 s79, s99, 0
	global_load_dword v46, v238, s[78:79] offset:640
	s_add_u32 s78, s98, s71
	s_addc_u32 s79, s99, 0
	global_load_dword v47, v238, s[78:79] offset:704
	s_add_u32 s78, s98, s72
	s_addc_u32 s79, s99, 0
	global_load_dword v48, v238, s[78:79] offset:768
	s_add_u32 s78, s98, s73
	s_addc_u32 s79, s99, 0
	global_load_dword v49, v238, s[78:79] offset:832
	s_add_u32 s78, s98, s74
	s_addc_u32 s79, s99, 0
	global_load_dword v50, v238, s[78:79] offset:896
	s_add_u32 s78, s98, s75
	s_addc_u32 s79, s99, 0
	global_load_dword v51, v238, s[78:79] offset:960
	s_waitcnt vmcnt(30)
	v_bfe_u32 v57, v31, 16, 16
	s_waitcnt vmcnt(29)
	v_bfe_u32 v62, v30, 16, 16
	s_waitcnt vmcnt(28)
	v_bfe_u32 v63, v29, 16, 16
	s_waitcnt vmcnt(27)
	v_bfe_u32 v64, v28, 16, 16
	v_perm_b32 v85, v31, v31, s63
	v_perm_b32 v86, v30, v30, s63
	v_perm_b32 v87, v29, v29, s63
	v_perm_b32 v88, v28, v28, s63
	v_cvt_f32_f16_e32 v28, v60
	v_cvt_f32_f16_sdwa v29, v60 dst_sel:DWORD dst_unused:UNUSED_PAD src0_sel:WORD_1
	v_cvt_f32_f16_e32 v30, v61
	v_cvt_f32_f16_sdwa v31, v61 dst_sel:DWORD dst_unused:UNUSED_PAD src0_sel:WORD_1
	v_bfe_u32 v56, v24, 16, 16
	s_waitcnt vmcnt(26)
	v_bfe_u32 v65, v27, 16, 16
	s_waitcnt vmcnt(25)
	v_bfe_u32 v66, v26, 16, 16
	s_waitcnt vmcnt(24)
	v_bfe_u32 v67, v25, 16, 16
	s_waitcnt vmcnt(23)
	v_bfe_u32 v68, v54, 16, 16
	s_waitcnt vmcnt(22)
	v_bfe_u32 v69, v53, 16, 16
	s_waitcnt vmcnt(21)
	v_bfe_u32 v70, v52, 16, 16
	s_waitcnt vmcnt(20)
	v_bfe_u32 v71, v35, 16, 16
	s_waitcnt vmcnt(19)
	v_bfe_u32 v72, v34, 16, 16
	s_waitcnt vmcnt(18)
	v_bfe_u32 v73, v33, 16, 16
	s_waitcnt vmcnt(17)
	v_bfe_u32 v74, v32, 16, 16
	s_waitcnt vmcnt(16)
	v_bfe_u32 v75, v55, 16, 16
	v_perm_b32 v84, v24, v24, s63
	v_perm_b32 v91, v25, v25, s63
	v_perm_b32 v92, v54, v54, s63
	v_perm_b32 v94, v52, v52, s63
	v_perm_b32 v96, v34, v34, s63
	v_perm_b32 v98, v32, v32, s63
	v_cvt_f32_f16_e32 v24, v58
	v_cvt_f32_f16_sdwa v25, v58 dst_sel:DWORD dst_unused:UNUSED_PAD src0_sel:WORD_1
	v_lshl_add_u32 v32, v56, 3, 0
	v_lshl_add_u32 v34, v57, 3, 0
	v_lshl_add_u32 v52, v62, 3, 0
	v_lshl_add_u32 v54, v63, 3, 0
	v_lshl_add_u32 v56, v64, 3, 0
	v_lshl_add_u32 v58, v65, 3, 0
	v_lshl_add_u32 v60, v66, 3, 0
	v_lshl_add_u32 v62, v67, 3, 0
	v_lshl_add_u32 v64, v68, 3, 0
	v_lshl_add_u32 v66, v69, 3, 0
	v_lshl_add_u32 v68, v70, 3, 0
	v_lshl_add_u32 v70, v71, 3, 0
	v_lshl_add_u32 v72, v72, 3, 0
	v_lshl_add_u32 v76, v73, 3, 0
	v_lshl_add_u32 v77, v74, 3, 0
	v_lshl_add_u32 v78, v75, 3, 0
	v_perm_b32 v89, v27, v27, s63
	v_perm_b32 v90, v26, v26, s63
	v_perm_b32 v93, v53, v53, s63
	v_perm_b32 v95, v35, v35, s63
	v_perm_b32 v97, v33, v33, s63
	v_perm_b32 v99, v55, v55, s63
	v_cvt_f32_f16_e32 v26, v59
	v_cvt_f32_f16_sdwa v27, v59 dst_sel:DWORD dst_unused:UNUSED_PAD src0_sel:WORD_1
	ds_read_b64 v[32:33], v32
	ds_read_b64 v[34:35], v34
	ds_read_b64 v[52:53], v52
	ds_read_b64 v[54:55], v54
	ds_read_b64 v[56:57], v56
	ds_read_b64 v[58:59], v58
	ds_read_b64 v[60:61], v60
	ds_read_b64 v[62:63], v62
	ds_read_b64 v[64:65], v64
	ds_read_b64 v[66:67], v66
	ds_read_b64 v[68:69], v68
	ds_read_b64 v[70:71], v70
	ds_read_b64 v[72:73], v72
	ds_read_b64 v[74:75], v76
	ds_read_b64 v[76:77], v77
	ds_read_b64 v[78:79], v78
	v_pk_add_f32 v[22:23], v[22:23], v[28:29]
	v_pk_add_f32 v[20:21], v[20:21], v[30:31]
	s_waitcnt lgkmcnt(14)
	v_perm_b32 v28, 0, v32, v169
	v_perm_b32 v29, 0, v32, v170
	v_perm_b32 v30, 0, v33, v169
	v_perm_b32 v31, 0, v33, v170
	v_perm_b32 v32, 0, v34, v169
	v_perm_b32 v33, 0, v34, v170
	v_perm_b32 v34, 0, v35, v169
	v_perm_b32 v35, 0, v35, v170
	v_pk_fma_f16 v28, v84, v28, 0
	v_pk_fma_f16 v29, v84, v29, 0
	v_pk_fma_f16 v30, v84, v30, 0
	v_pk_fma_f16 v31, v84, v31, 0
	s_waitcnt lgkmcnt(13)
	v_perm_b32 v100, 0, v52, v169
	v_perm_b32 v52, 0, v52, v170
	v_perm_b32 v101, 0, v53, v169
	v_perm_b32 v53, 0, v53, v170
	v_pk_fma_f16 v28, v85, v32, v28
	v_pk_fma_f16 v29, v85, v33, v29
	v_pk_fma_f16 v30, v85, v34, v30
	v_pk_fma_f16 v31, v85, v35, v31
	s_waitcnt lgkmcnt(12)
	v_perm_b32 v102, 0, v54, v169
	v_perm_b32 v54, 0, v54, v170
	v_perm_b32 v103, 0, v55, v169
	v_perm_b32 v55, 0, v55, v170
	v_pk_fma_f16 v28, v86, v100, v28
	v_pk_fma_f16 v29, v86, v52, v29
	v_pk_fma_f16 v30, v86, v101, v30
	v_pk_fma_f16 v31, v86, v53, v31
	s_waitcnt lgkmcnt(11)
	v_perm_b32 v104, 0, v56, v169
	v_perm_b32 v56, 0, v56, v170
	v_perm_b32 v105, 0, v57, v169
	v_perm_b32 v57, 0, v57, v170
	v_pk_fma_f16 v28, v87, v102, v28
	v_pk_fma_f16 v29, v87, v54, v29
	v_pk_fma_f16 v30, v87, v103, v30
	v_pk_fma_f16 v31, v87, v55, v31
	s_waitcnt lgkmcnt(10)
	v_perm_b32 v106, 0, v58, v169
	v_perm_b32 v58, 0, v58, v170
	v_perm_b32 v107, 0, v59, v169
	v_perm_b32 v59, 0, v59, v170
	v_pk_fma_f16 v28, v88, v104, v28
	v_pk_fma_f16 v29, v88, v56, v29
	v_pk_fma_f16 v30, v88, v105, v30
	v_pk_fma_f16 v31, v88, v57, v31
	s_waitcnt lgkmcnt(9)
; #define VL_LOAD(wr, C) do { _Pragma("unroll") for (int i = 0; i < 16; ++i) wr[i] = wp[(size_t)((C) * 16 + i) * MROWS]; } while (0)
; #define VL_LOAD(wr, C) do { _Pragma("unroll") for (int i = 0; i < 16; ++i) wr[i] = wp[(size_t)((C) * 16 + i) * MROWS]; } while (0)
; template <bool RUN_L = true, bool RUN_G = true, bool DRY = false>
; __device__ __forceinline__ void phase_vaccH(unsigned char* ws, LAS unsigned char* lds, int layer, int G) {
;     ...
; #pragma unroll 1
;             for (int tb = wid; tb < NTB; tb += 4) {
;                 const int tok = tb * 64 + lane; const bool valid = tok < MROWS; const int tokc = valid ? tok : MROWS - 1;
;                 const unsigned* wp = WLT + tokc;
;                 f32x4* hp = (f32x4*)(H + (size_t)tokc * D + cg * 8); const f32x4 h0 = hp[0], h1 = hp[1];
;                 float accf[8];
; #pragma unroll
;                 for (int j = 0; j < 8; ++j) accf[j] = 0.f;
;                 unsigned wa[16], wb[16];
;                 VL_LOAD(wa, 0);
; #pragma unroll 1
;                 for (int c = 0; c < 8; c += 2) {
;                     VL_LOAD(wb, c + 1);
;                     __builtin_amdgcn_sched_barrier(0);
;                     VL_CHUNK(wa);
;                     __builtin_amdgcn_sched_barrier(0);
;                     VL_LOAD(wa, (c + 2) & 7);
;                     __builtin_amdgcn_sched_barrier(0);
;                     VL_CHUNK(wb);
;                     __builtin_amdgcn_sched_barrier(0);
;                 }
;                 if (valid) { hp[0] = h0 + (f32x4){accf[0], accf[1], accf[2], accf[3]}; hp[1] = h1 + (f32x4){accf[4], accf[5], accf[6], accf[7]}; }
	v_perm_b32 v108, 0, v60, v169
	v_perm_b32 v60, 0, v60, v170
	v_perm_b32 v109, 0, v61, v169
	v_perm_b32 v61, 0, v61, v170
	v_pk_fma_f16 v28, v89, v106, v28
	v_pk_fma_f16 v29, v89, v58, v29
	v_pk_fma_f16 v30, v89, v107, v30
	v_pk_fma_f16 v31, v89, v59, v31
	s_waitcnt lgkmcnt(8)
	v_perm_b32 v110, 0, v62, v169
	v_perm_b32 v62, 0, v62, v170
	v_perm_b32 v111, 0, v63, v169
	v_perm_b32 v63, 0, v63, v170
	v_pk_fma_f16 v28, v90, v108, v28
	v_pk_fma_f16 v29, v90, v60, v29
	v_pk_fma_f16 v30, v90, v109, v30
	v_pk_fma_f16 v31, v90, v61, v31
	s_waitcnt lgkmcnt(7)
	v_perm_b32 v112, 0, v64, v169
	v_perm_b32 v64, 0, v64, v170
	v_perm_b32 v113, 0, v65, v169
	v_perm_b32 v65, 0, v65, v170
	v_pk_fma_f16 v28, v91, v110, v28
	v_pk_fma_f16 v29, v91, v62, v29
	v_pk_fma_f16 v30, v91, v111, v30
	v_pk_fma_f16 v31, v91, v63, v31
	s_waitcnt lgkmcnt(6)
	v_perm_b32 v114, 0, v66, v169
	v_perm_b32 v66, 0, v66, v170
	v_perm_b32 v115, 0, v67, v169
	v_perm_b32 v67, 0, v67, v170
	v_pk_fma_f16 v28, v92, v112, v28
	v_pk_fma_f16 v29, v92, v64, v29
	v_pk_fma_f16 v30, v92, v113, v30
	v_pk_fma_f16 v31, v92, v65, v31
	s_waitcnt lgkmcnt(5)
	v_perm_b32 v116, 0, v68, v169
	v_perm_b32 v68, 0, v68, v170
	v_perm_b32 v117, 0, v69, v169
	v_perm_b32 v69, 0, v69, v170
	v_pk_fma_f16 v28, v93, v114, v28
	v_pk_fma_f16 v29, v93, v66, v29
	v_pk_fma_f16 v30, v93, v115, v30
	v_pk_fma_f16 v31, v93, v67, v31
	s_waitcnt lgkmcnt(4)
	v_perm_b32 v118, 0, v70, v169
	v_perm_b32 v70, 0, v70, v170
	v_perm_b32 v119, 0, v71, v169
	v_perm_b32 v71, 0, v71, v170
	v_pk_fma_f16 v28, v94, v116, v28
	v_pk_fma_f16 v29, v94, v68, v29
	v_pk_fma_f16 v30, v94, v117, v30
	v_pk_fma_f16 v31, v94, v69, v31
	s_waitcnt lgkmcnt(3)
	v_perm_b32 v120, 0, v72, v169
	v_perm_b32 v72, 0, v72, v170
	v_perm_b32 v121, 0, v73, v169
	v_perm_b32 v73, 0, v73, v170
	v_pk_fma_f16 v28, v95, v118, v28
	v_pk_fma_f16 v29, v95, v70, v29
	v_pk_fma_f16 v30, v95, v119, v30
	v_pk_fma_f16 v31, v95, v71, v31
	s_waitcnt lgkmcnt(2)
	v_perm_b32 v122, 0, v74, v169
	v_perm_b32 v74, 0, v74, v170
	v_perm_b32 v123, 0, v75, v169
	v_perm_b32 v75, 0, v75, v170
	v_pk_fma_f16 v28, v96, v120, v28
	v_pk_fma_f16 v29, v96, v72, v29
	v_pk_fma_f16 v30, v96, v121, v30
	v_pk_fma_f16 v31, v96, v73, v31
	s_waitcnt lgkmcnt(1)
	v_perm_b32 v124, 0, v76, v169
	v_perm_b32 v76, 0, v76, v170
	v_perm_b32 v125, 0, v77, v169
	v_perm_b32 v77, 0, v77, v170
	v_pk_fma_f16 v28, v97, v122, v28
	v_pk_fma_f16 v29, v97, v74, v29
	v_pk_fma_f16 v30, v97, v123, v30
	v_pk_fma_f16 v31, v97, v75, v31
	s_waitcnt lgkmcnt(0)
	v_perm_b32 v126, 0, v78, v169
	v_perm_b32 v78, 0, v78, v170
	v_perm_b32 v127, 0, v79, v169
	v_perm_b32 v79, 0, v79, v170
	v_pk_fma_f16 v28, v98, v124, v28
	v_pk_fma_f16 v29, v98, v76, v29
	v_pk_fma_f16 v30, v98, v125, v30
	v_pk_fma_f16 v31, v98, v77, v31
	v_pk_fma_f16 v33, v99, v126, v28
	v_pk_fma_f16 v52, v99, v78, v29
	v_pk_fma_f16 v29, v99, v127, v30
	v_pk_fma_f16 v31, v99, v79, v31
	v_cvt_f32_f16_e32 v32, v33
	v_cvt_f32_f16_e32 v30, v52
	v_cvt_f32_f16_e32 v28, v29
	v_cvt_f32_f16_e32 v34, v31
	v_cvt_f32_f16_sdwa v35, v31 dst_sel:DWORD dst_unused:UNUSED_PAD src0_sel:WORD_1
	v_cvt_f32_f16_sdwa v29, v29 dst_sel:DWORD dst_unused:UNUSED_PAD src0_sel:WORD_1
	v_cvt_f32_f16_sdwa v31, v52 dst_sel:DWORD dst_unused:UNUSED_PAD src0_sel:WORD_1
	v_cvt_f32_f16_sdwa v33, v33 dst_sel:DWORD dst_unused:UNUSED_PAD src0_sel:WORD_1
	v_pk_add_f32 v[80:81], v[18:19], v[24:25]
	v_pk_add_f32 v[82:83], v[16:17], v[26:27]
	v_pk_add_f32 v[20:21], v[20:21], v[34:35]
	v_pk_add_f32 v[22:23], v[22:23], v[28:29]
	v_pk_add_f32 v[34:35], v[82:83], v[30:31]
	v_pk_add_f32 v[28:29], v[80:81], v[32:33]
	s_add_u32 s76, s76, s20
	s_addc_u32 s77, s77, s21
	s_add_i32 s46, s46, 32
	s_add_i32 s47, s47, 2
	s_cmp_lt_u32 s47, 6
	v_lshl_add_u64 v[14:15], v[14:15], 0, s[20:21]
	s_cbranch_scc1 .LBB0_1242
	s_and_saveexec_b64 s[46:47], s[6:7]
	v_pk_add_f32 v[12:13], v[18:19], v[24:25]
	v_pk_add_f32 v[14:15], v[16:17], v[26:27]
	v_pk_add_f32 v[12:13], v[12:13], v[32:33]
	v_pk_add_f32 v[14:15], v[14:15], v[30:31]
	v_pk_add_f32 v[6:7], v[6:7], v[12:13]
	v_pk_add_f32 v[8:9], v[8:9], v[14:15]
	v_pk_add_f32 v[4:5], v[4:5], v[20:21]
	v_pk_add_f32 v[2:3], v[2:3], v[22:23]
	global_store_dwordx4 v[10:11], v[6:9], off
	global_store_dwordx4 v[10:11], v[2:5], off offset:16
	s_branch .LBB0_1240

; #define VL_LOAD(wr, C) do { _Pragma("unroll") for (int i = 0; i < 16; ++i) wr[i] = wp[(size_t)((C) * 16 + i) * MROWS]; } while (0)
; #define VL_LOAD(wr, C) do { _Pragma("unroll") for (int i = 0; i < 16; ++i) wr[i] = wp[(size_t)((C) * 16 + i) * MROWS]; } while (0)
; template <bool RUN_L = true, bool RUN_G = true, bool DRY = false>
; __device__ __forceinline__ void phase_vaccH(unsigned char* ws, LAS unsigned char* lds, int layer, int G) {
;     ...
;             for (int tb = wid; tb < NTB; tb += 4) {
;                 const int tok = tb * 64 + lane; const bool valid = tok < MROWS; const int tokc = valid ? tok : MROWS - 1;
;                 const unsigned* wp = WLT + tokc;
;                 f32x4* hp = (f32x4*)(H + (size_t)tokc * D + cg * 8); const f32x4 h0 = hp[0], h1 = hp[1];
;                 float accf[8];
; #pragma unroll
;                 for (int j = 0; j < 8; ++j) accf[j] = 0.f;
;                 unsigned wa[16], wb[16];
;                 VL_LOAD(wa, 0);
; #pragma unroll 1
;                 for (int c = 0; c < 8; c += 2) {
;                     VL_LOAD(wb, c + 1);
;                     __builtin_amdgcn_sched_barrier(0);
;                     VL_CHUNK(wa);
.LBB0_1986:
	s_waitcnt vmcnt(2)
	v_lshl_or_b32 v2, s23, 6, v1
	v_cmp_gt_i32_e64 s[6:7], s39, v2
	s_mov_b32 s30, 32
	s_mov_b32 s31, -2
	v_cndmask_b32_e64 v12, v171, v2, s[6:7]
	v_ashrrev_i32_e32 v13, 31, v12
	v_lshlrev_b64 v[14:15], 2, v[12:13]
	v_mov_b32_e32 v238, v14
	v_lshlrev_b64 v[2:3], 14, v[12:13]
	v_lshl_add_u64 v[12:13], s[16:17], 0, v[14:15]
	v_lshl_add_u64 v[10:11], s[28:29], 0, v[2:3]
	global_load_dwordx4 v[2:5], v[10:11], off offset:16
	global_load_dwordx4 v[6:9], v[10:11], off
	v_lshl_add_u64 v[14:15], s[18:19], 0, v[14:15]
	s_mov_b64 s[76:77], s[18:19]
	global_load_dword v46, v238, s[16:17]
	s_add_u32 s78, s16, s52
	s_addc_u32 s79, s17, 0
	global_load_dword v44, v238, s[78:79] offset:64
	s_add_u32 s78, s16, s41
	s_addc_u32 s79, s17, 0
	global_load_dword v42, v238, s[78:79] offset:128
	s_add_u32 s78, s16, s45
	s_addc_u32 s79, s17, 0
	global_load_dword v40, v238, s[78:79] offset:192
	s_add_u32 s78, s16, s54
	s_addc_u32 s79, s17, 0
	global_load_dword v39, v238, s[78:79] offset:256
	s_add_u32 s78, s16, s55
	s_addc_u32 s79, s17, 0
	global_load_dword v38, v238, s[78:79] offset:320
	s_add_u32 s78, s16, s56
	s_addc_u32 s79, s17, 0
	global_load_dword v37, v238, s[78:79] offset:384
	s_add_u32 s78, s16, s57
	s_addc_u32 s79, s17, 0
	global_load_dword v36, v238, s[78:79] offset:448
	s_add_u32 s78, s16, s58
	s_addc_u32 s79, s17, 0
	global_load_dword v51, v238, s[78:79] offset:512
	s_add_u32 s78, s16, s59
	s_addc_u32 s79, s17, 0
	global_load_dword v50, v238, s[78:79] offset:576
	s_add_u32 s78, s16, s60
	s_addc_u32 s79, s17, 0
	global_load_dword v49, v238, s[78:79] offset:640
	s_add_u32 s78, s16, s61
	s_addc_u32 s79, s17, 0
	global_load_dword v48, v238, s[78:79] offset:704
	s_add_u32 s78, s16, s62
	s_addc_u32 s79, s17, 0
	global_load_dword v47, v238, s[78:79] offset:768
	s_add_u32 s78, s16, 0x68000
	s_addc_u32 s79, s17, 0
	global_load_dword v45, v238, s[78:79] offset:832
	s_add_u32 s78, s16, 0x70000
	s_addc_u32 s79, s17, 0
	global_load_dword v43, v238, s[78:79] offset:896
	s_add_u32 s78, s16, 0x78000
	s_addc_u32 s79, s17, 0
	global_load_dword v41, v238, s[78:79] offset:960
	v_mov_b32_e32 v28, 0
	v_mov_b32_e32 v29, v28
	v_mov_b32_e32 v30, v28
	v_mov_b32_e32 v31, v28
	v_mov_b32_e32 v22, v28
	v_mov_b32_e32 v23, v28
	v_mov_b32_e32 v20, v28
	v_mov_b32_e32 v21, v28
.LBB0_1987:
	s_add_u32 s78, s76, s52
	s_addc_u32 s79, s77, 0
	global_load_dword v72, v238, s[78:79] offset:64
	s_add_u32 s78, s76, s41
	s_addc_u32 s79, s77, 0
	global_load_dword v73, v238, s[78:79] offset:128
	s_add_u32 s78, s76, s45
	s_addc_u32 s79, s77, 0
	global_load_dword v74, v238, s[78:79] offset:192
	s_add_u32 s78, s76, s54
	s_addc_u32 s79, s77, 0
	global_load_dword v75, v238, s[78:79] offset:256
	s_add_u32 s78, s76, s55
	s_addc_u32 s79, s77, 0
	global_load_dword v76, v238, s[78:79] offset:320
	s_add_u32 s78, s76, s56
	s_addc_u32 s79, s77, 0
	global_load_dword v77, v238, s[78:79] offset:384
	s_add_u32 s78, s76, s57
	s_addc_u32 s79, s77, 0
	global_load_dword v78, v238, s[78:79] offset:448
	s_add_u32 s78, s76, s58
	s_addc_u32 s79, s77, 0
	global_load_dword v79, v238, s[78:79] offset:512
	global_load_dword v80, v238, s[76:77]
	s_add_u32 s78, s76, s59
	s_addc_u32 s79, s77, 0
	global_load_dword v81, v238, s[78:79] offset:576
	s_add_u32 s78, s76, s60
	s_addc_u32 s79, s77, 0
	global_load_dword v82, v238, s[78:79] offset:640
	s_add_u32 s78, s76, s61
	s_addc_u32 s79, s77, 0
	global_load_dword v83, v238, s[78:79] offset:704
	s_add_u32 s78, s76, s62
	s_addc_u32 s79, s77, 0
	global_load_dword v84, v238, s[78:79] offset:768
	s_add_u32 s78, s76, s63
	s_addc_u32 s79, s77, 0
	global_load_dword v85, v238, s[78:79] offset:832
	s_add_u32 s78, s76, s64
	s_addc_u32 s79, s77, 0
	global_load_dword v86, v238, s[78:79] offset:896
	s_add_u32 s78, s76, s65
	s_addc_u32 s79, s77, 0
	global_load_dword v87, v238, s[78:79] offset:960
	v_mov_b32_e32 v17, v31
	v_mov_b32_e32 v16, v30
	v_mov_b32_e32 v19, v29
	v_mov_b32_e32 v18, v28
	s_waitcnt vmcnt(30)
	v_bfe_u32 v25, v44, 16, 16
	v_lshl_add_u32 v26, v25, 3, 0
	s_waitcnt vmcnt(29)
	v_bfe_u32 v25, v42, 16, 16
	v_bfe_u32 v24, v46, 16, 16
	v_lshl_add_u32 v28, v25, 3, 0
	s_waitcnt vmcnt(28)
	v_bfe_u32 v25, v40, 16, 16
	v_lshl_add_u32 v24, v24, 3, 0
	v_lshl_add_u32 v30, v25, 3, 0
	ds_read_b64 v[24:25], v24
	ds_read_b64 v[26:27], v26
	ds_read_b64 v[28:29], v28
	ds_read_b64 v[30:31], v30
	v_perm_b32 v46, v46, v46, s53
	s_waitcnt lgkmcnt(3)
	v_perm_b32 v88, 0, v24, v169
	v_perm_b32 v24, 0, v24, v170
	v_perm_b32 v89, 0, v25, v169
	v_perm_b32 v25, 0, v25, v170
	v_pk_fma_f16 v88, v46, v88, 0
	v_pk_fma_f16 v24, v46, v24, 0
	v_pk_fma_f16 v89, v46, v89, 0
	v_pk_fma_f16 v25, v46, v25, 0
	v_perm_b32 v44, v44, v44, s53
	s_waitcnt lgkmcnt(2)
	v_perm_b32 v46, 0, v26, v169
	v_perm_b32 v26, 0, v26, v170
	v_pk_fma_f16 v24, v44, v26, v24
	v_perm_b32 v26, 0, v27, v169
	v_perm_b32 v27, 0, v27, v170
	s_waitcnt vmcnt(26)
	v_bfe_u32 v33, v38, 16, 16
	v_pk_fma_f16 v25, v44, v27, v25
	v_perm_b32 v27, v42, v42, s53
	s_waitcnt lgkmcnt(1)
	v_perm_b32 v42, 0, v28, v169
	v_perm_b32 v28, 0, v28, v170
	v_lshl_add_u32 v34, v33, 3, 0
	s_waitcnt vmcnt(25)
	v_bfe_u32 v33, v37, 16, 16
	v_pk_fma_f16 v26, v44, v26, v89
	v_pk_fma_f16 v24, v27, v28, v24
	v_perm_b32 v28, 0, v29, v169
	v_bfe_u32 v32, v39, 16, 16
	v_lshl_add_u32 v52, v33, 3, 0
	s_waitcnt vmcnt(24)
	v_bfe_u32 v33, v36, 16, 16
	v_pk_fma_f16 v46, v44, v46, v88
	v_pk_fma_f16 v26, v27, v28, v26
	v_perm_b32 v28, 0, v29, v170
	v_lshl_add_u32 v32, v32, 3, 0
	v_lshl_add_u32 v54, v33, 3, 0
	v_pk_fma_f16 v42, v27, v42, v46
	v_pk_fma_f16 v25, v27, v28, v25
	v_perm_b32 v27, v40, v40, s53
	s_waitcnt lgkmcnt(0)
; #define VL_LOAD(wr, C) do { _Pragma("unroll") for (int i = 0; i < 16; ++i) wr[i] = wp[(size_t)((C) * 16 + i) * MROWS]; } while (0)
; #define VL_LOAD(wr, C) do { _Pragma("unroll") for (int i = 0; i < 16; ++i) wr[i] = wp[(size_t)((C) * 16 + i) * MROWS]; } while (0)
; template <bool RUN_L = true, bool RUN_G = true, bool DRY = false>
; __device__ __forceinline__ void phase_vaccH(unsigned char* ws, LAS unsigned char* lds, int layer, int G) {
;     ...
; #pragma unroll 1
;             for (int tb = wid; tb < NTB; tb += 4) {
;                 const int tok = tb * 64 + lane; const bool valid = tok < MROWS; const int tokc = valid ? tok : MROWS - 1;
;                 const unsigned* wp = WLT + tokc;
;                 f32x4* hp = (f32x4*)(H + (size_t)tokc * D + cg * 8); const f32x4 h0 = hp[0], h1 = hp[1];
;                 float accf[8];
; #pragma unroll
;                 for (int j = 0; j < 8; ++j) accf[j] = 0.f;
;                 unsigned wa[16], wb[16];
;                 VL_LOAD(wa, 0);
; #pragma unroll 1
;                 for (int c = 0; c < 8; c += 2) {
;                     VL_LOAD(wb, c + 1);
;                     __builtin_amdgcn_sched_barrier(0);
;                     VL_CHUNK(wa);
;                     __builtin_amdgcn_sched_barrier(0);
;                     VL_LOAD(wa, (c + 2) & 7);
	v_perm_b32 v29, 0, v30, v170
	ds_read_b64 v[32:33], v32
	ds_read_b64 v[34:35], v34
	ds_read_b64 v[52:53], v52
	ds_read_b64 v[54:55], v54
	v_pk_fma_f16 v24, v27, v29, v24
	v_perm_b32 v29, 0, v31, v169
	v_perm_b32 v28, 0, v30, v169
	v_pk_fma_f16 v26, v27, v29, v26
	v_perm_b32 v29, 0, v31, v170
	v_pk_fma_f16 v28, v27, v28, v42
	v_pk_fma_f16 v25, v27, v29, v25
	v_perm_b32 v27, v39, v39, s53
	s_waitcnt lgkmcnt(3)
	v_perm_b32 v29, 0, v32, v169
	v_pk_fma_f16 v28, v27, v29, v28
	v_perm_b32 v29, 0, v32, v170
	v_pk_fma_f16 v24, v27, v29, v24
	v_perm_b32 v29, 0, v33, v169
	v_pk_fma_f16 v26, v27, v29, v26
	v_perm_b32 v29, 0, v33, v170
	v_pk_fma_f16 v25, v27, v29, v25
	v_perm_b32 v27, v38, v38, s53
	s_waitcnt lgkmcnt(2)
	v_perm_b32 v29, 0, v34, v169
	v_pk_fma_f16 v28, v27, v29, v28
	v_perm_b32 v29, 0, v34, v170
	v_pk_fma_f16 v24, v27, v29, v24
	v_perm_b32 v29, 0, v35, v169
	v_pk_fma_f16 v26, v27, v29, v26
	v_perm_b32 v29, 0, v35, v170
	v_pk_fma_f16 v25, v27, v29, v25
	v_perm_b32 v27, v37, v37, s53
	s_waitcnt lgkmcnt(1)
	v_perm_b32 v29, 0, v52, v169
	v_pk_fma_f16 v28, v27, v29, v28
	v_perm_b32 v29, 0, v52, v170
	s_waitcnt vmcnt(22)
	v_bfe_u32 v57, v50, 16, 16
	v_pk_fma_f16 v24, v27, v29, v24
	v_perm_b32 v29, 0, v53, v169
	v_lshl_add_u32 v58, v57, 3, 0
	s_waitcnt vmcnt(21)
	v_bfe_u32 v57, v49, 16, 16
	v_pk_fma_f16 v26, v27, v29, v26
	v_perm_b32 v29, 0, v53, v170
	v_bfe_u32 v56, v51, 16, 16
	v_lshl_add_u32 v60, v57, 3, 0
	s_waitcnt vmcnt(20)
	v_bfe_u32 v57, v48, 16, 16
	v_pk_fma_f16 v25, v27, v29, v25
	v_perm_b32 v27, v36, v36, s53
	s_waitcnt lgkmcnt(0)
	v_perm_b32 v29, 0, v54, v169
	v_lshl_add_u32 v56, v56, 3, 0
	v_lshl_add_u32 v62, v57, 3, 0
	v_pk_fma_f16 v28, v27, v29, v28
	v_perm_b32 v29, 0, v54, v170
	ds_read_b64 v[56:57], v56
	ds_read_b64 v[58:59], v58
	ds_read_b64 v[60:61], v60
	ds_read_b64 v[62:63], v62
	v_pk_fma_f16 v24, v27, v29, v24
	v_perm_b32 v29, 0, v55, v169
	v_pk_fma_f16 v26, v27, v29, v26
	v_perm_b32 v29, 0, v55, v170
	v_pk_fma_f16 v25, v27, v29, v25
	v_perm_b32 v27, v51, v51, s53
	s_waitcnt lgkmcnt(3)
	v_perm_b32 v29, 0, v56, v169
	v_pk_fma_f16 v28, v27, v29, v28
	v_perm_b32 v29, 0, v56, v170
	v_pk_fma_f16 v24, v27, v29, v24
	v_perm_b32 v29, 0, v57, v169
	v_pk_fma_f16 v26, v27, v29, v26
	v_perm_b32 v29, 0, v57, v170
	v_pk_fma_f16 v25, v27, v29, v25
	v_perm_b32 v27, v50, v50, s53
	s_waitcnt lgkmcnt(2)
	v_perm_b32 v29, 0, v58, v169
	v_pk_fma_f16 v28, v27, v29, v28
	v_perm_b32 v29, 0, v58, v170
	v_pk_fma_f16 v24, v27, v29, v24
	v_perm_b32 v29, 0, v59, v169
	v_pk_fma_f16 v26, v27, v29, v26
	v_perm_b32 v29, 0, v59, v170
	v_pk_fma_f16 v25, v27, v29, v25
	v_perm_b32 v27, v49, v49, s53
	s_waitcnt lgkmcnt(1)
	v_perm_b32 v29, 0, v60, v169
	v_pk_fma_f16 v28, v27, v29, v28
	v_perm_b32 v29, 0, v60, v170
	s_waitcnt vmcnt(18)
	v_bfe_u32 v65, v45, 16, 16
	v_pk_fma_f16 v24, v27, v29, v24
	v_perm_b32 v29, 0, v61, v169
	v_lshl_add_u32 v66, v65, 3, 0
	s_waitcnt vmcnt(17)
	v_bfe_u32 v65, v43, 16, 16
	v_pk_fma_f16 v26, v27, v29, v26
	v_perm_b32 v29, 0, v61, v170
	v_bfe_u32 v64, v47, 16, 16
	v_lshl_add_u32 v68, v65, 3, 0
	s_waitcnt vmcnt(16)
	v_bfe_u32 v65, v41, 16, 16
	v_pk_fma_f16 v25, v27, v29, v25
	v_perm_b32 v27, v48, v48, s53
	s_waitcnt lgkmcnt(0)
	v_perm_b32 v29, 0, v62, v169
	v_lshl_add_u32 v64, v64, 3, 0
	v_lshl_add_u32 v70, v65, 3, 0
	v_pk_fma_f16 v28, v27, v29, v28
	v_perm_b32 v29, 0, v62, v170
	ds_read_b64 v[64:65], v64
	ds_read_b64 v[66:67], v66
	ds_read_b64 v[68:69], v68
	ds_read_b64 v[70:71], v70
	v_pk_fma_f16 v24, v27, v29, v24
	v_perm_b32 v29, 0, v63, v169
	v_pk_fma_f16 v26, v27, v29, v26
	v_perm_b32 v29, 0, v63, v170
	v_pk_fma_f16 v25, v27, v29, v25
	v_perm_b32 v27, v47, v47, s53
	s_waitcnt lgkmcnt(3)
	v_perm_b32 v29, 0, v64, v169
	v_pk_fma_f16 v28, v27, v29, v28
	v_perm_b32 v29, 0, v64, v170
	v_pk_fma_f16 v24, v27, v29, v24
	v_perm_b32 v29, 0, v65, v169
	v_pk_fma_f16 v26, v27, v29, v26
	v_perm_b32 v29, 0, v65, v170
	v_pk_fma_f16 v25, v27, v29, v25
	v_perm_b32 v27, v45, v45, s53
	s_waitcnt lgkmcnt(2)
	v_perm_b32 v29, 0, v66, v169
	v_pk_fma_f16 v28, v27, v29, v28
	v_perm_b32 v29, 0, v66, v170
	v_pk_fma_f16 v24, v27, v29, v24
	v_perm_b32 v29, 0, v67, v169
	v_pk_fma_f16 v26, v27, v29, v26
	v_perm_b32 v29, 0, v67, v170
	v_pk_fma_f16 v25, v27, v29, v25
	v_perm_b32 v27, v43, v43, s53
	s_waitcnt lgkmcnt(1)
	v_perm_b32 v29, 0, v68, v169
	v_pk_fma_f16 v28, v27, v29, v28
	v_perm_b32 v29, 0, v68, v170
	v_pk_fma_f16 v24, v27, v29, v24
	v_perm_b32 v29, 0, v69, v169
	v_pk_fma_f16 v26, v27, v29, v26
	v_perm_b32 v29, 0, v69, v170
	v_pk_fma_f16 v25, v27, v29, v25
	v_perm_b32 v27, v41, v41, s53
	s_waitcnt lgkmcnt(0)
	v_perm_b32 v29, 0, v70, v169
	v_pk_fma_f16 v56, v27, v29, v28
	v_perm_b32 v28, 0, v70, v170
	v_pk_fma_f16 v57, v27, v28, v24
	v_perm_b32 v24, 0, v71, v169
	v_pk_fma_f16 v58, v27, v24, v26
	v_perm_b32 v24, 0, v71, v170
	v_pk_fma_f16 v59, v27, v24, v25
	s_and_b32 s8, s30, 0x60
	s_mul_i32 s8, s8, 0x8040
	s_add_u32 s98, s16, s8
	s_addc_u32 s99, s17, 0
	global_load_dword v46, v238, s[98:99]
	s_add_u32 s78, s98, s52
	s_addc_u32 s79, s99, 0
	global_load_dword v44, v238, s[78:79] offset:64
	s_add_u32 s78, s98, s41
	s_addc_u32 s79, s99, 0
	global_load_dword v42, v238, s[78:79] offset:128
	s_add_u32 s78, s98, s45
	s_addc_u32 s79, s99, 0
	global_load_dword v40, v238, s[78:79] offset:192
	s_add_u32 s78, s98, s54
	s_addc_u32 s79, s99, 0
	global_load_dword v39, v238, s[78:79] offset:256
	s_add_u32 s78, s98, s55
	s_addc_u32 s79, s99, 0
	global_load_dword v38, v238, s[78:79] offset:320
	s_add_u32 s78, s98, s56
	s_addc_u32 s79, s99, 0
	global_load_dword v37, v238, s[78:79] offset:384
	s_add_u32 s78, s98, s57
	s_addc_u32 s79, s99, 0
	global_load_dword v36, v238, s[78:79] offset:448
	s_add_u32 s78, s98, s58
	s_addc_u32 s79, s99, 0
	global_load_dword v51, v238, s[78:79] offset:512
	s_add_u32 s78, s98, s59
	s_addc_u32 s79, s99, 0
	global_load_dword v50, v238, s[78:79] offset:576
	s_add_u32 s78, s98, s60
	s_addc_u32 s79, s99, 0
	global_load_dword v49, v238, s[78:79] offset:640
	s_add_u32 s78, s98, s61
	s_addc_u32 s79, s99, 0
	global_load_dword v48, v238, s[78:79] offset:704
	s_add_u32 s78, s98, s62
	s_addc_u32 s79, s99, 0
	global_load_dword v47, v238, s[78:79] offset:768
	s_add_u32 s78, s98, s63
	s_addc_u32 s79, s99, 0
	global_load_dword v45, v238, s[78:79] offset:832
	s_add_u32 s78, s98, s64
	s_addc_u32 s79, s99, 0
	global_load_dword v43, v238, s[78:79] offset:896
	s_add_u32 s78, s98, s65
	s_addc_u32 s79, s99, 0
	global_load_dword v41, v238, s[78:79] offset:960
	v_cvt_f32_f16_e32 v28, v58
	v_cvt_f32_f16_sdwa v29, v58 dst_sel:DWORD dst_unused:UNUSED_PAD src0_sel:WORD_1
	v_cvt_f32_f16_e32 v30, v59
	v_cvt_f32_f16_sdwa v31, v59 dst_sel:DWORD dst_unused:UNUSED_PAD src0_sel:WORD_1
	s_waitcnt vmcnt(23)
	v_bfe_u32 v32, v80, 16, 16
	v_bfe_u32 v33, v72, 16, 16
	v_bfe_u32 v34, v73, 16, 16
	v_bfe_u32 v35, v74, 16, 16
	v_bfe_u32 v52, v75, 16, 16
	v_bfe_u32 v53, v76, 16, 16
	v_bfe_u32 v54, v77, 16, 16
	v_bfe_u32 v55, v78, 16, 16
	v_bfe_u32 v60, v79, 16, 16
	s_waitcnt vmcnt(22)
	v_bfe_u32 v61, v81, 16, 16
	s_waitcnt vmcnt(21)
	v_bfe_u32 v62, v82, 16, 16
	s_waitcnt vmcnt(20)
	v_bfe_u32 v63, v83, 16, 16
	s_waitcnt vmcnt(19)
	v_bfe_u32 v64, v84, 16, 16
	s_waitcnt vmcnt(18)
	v_bfe_u32 v65, v85, 16, 16
	s_waitcnt vmcnt(17)
	v_bfe_u32 v66, v86, 16, 16
	s_waitcnt vmcnt(16)
	v_bfe_u32 v67, v87, 16, 16
	v_perm_b32 v89, v72, v72, s53
	v_perm_b32 v90, v73, v73, s53
	v_perm_b32 v91, v74, v74, s53
	v_perm_b32 v92, v75, v75, s53
	v_perm_b32 v93, v76, v76, s53
	v_perm_b32 v94, v77, v77, s53
	v_perm_b32 v95, v78, v78, s53
	v_cvt_f32_f16_e32 v24, v56
	v_cvt_f32_f16_sdwa v25, v56 dst_sel:DWORD dst_unused:UNUSED_PAD src0_sel:WORD_1
	v_cvt_f32_f16_e32 v26, v57
	v_cvt_f32_f16_sdwa v27, v57 dst_sel:DWORD dst_unused:UNUSED_PAD src0_sel:WORD_1
	v_lshl_add_u32 v32, v32, 3, 0
	v_lshl_add_u32 v56, v33, 3, 0
	v_lshl_add_u32 v57, v34, 3, 0
	v_lshl_add_u32 v58, v35, 3, 0
	v_lshl_add_u32 v59, v52, 3, 0
	v_lshl_add_u32 v68, v53, 3, 0
	v_lshl_add_u32 v69, v54, 3, 0
	v_lshl_add_u32 v70, v55, 3, 0
	v_lshl_add_u32 v71, v60, 3, 0
	v_lshl_add_u32 v72, v61, 3, 0
	v_lshl_add_u32 v73, v62, 3, 0
	v_lshl_add_u32 v74, v63, 3, 0
	v_lshl_add_u32 v75, v64, 3, 0
	v_lshl_add_u32 v76, v65, 3, 0
	v_lshl_add_u32 v77, v66, 3, 0
	v_lshl_add_u32 v78, v67, 3, 0
	v_perm_b32 v88, v80, v80, s53
	v_perm_b32 v96, v79, v79, s53
	ds_read_b64 v[32:33], v32
	ds_read_b64 v[34:35], v56
	ds_read_b64 v[52:53], v57
	ds_read_b64 v[54:55], v58
	ds_read_b64 v[56:57], v59
	ds_read_b64 v[58:59], v68
	ds_read_b64 v[60:61], v69
	ds_read_b64 v[62:63], v70
	ds_read_b64 v[64:65], v71
	ds_read_b64 v[66:67], v72
	ds_read_b64 v[68:69], v73
	ds_read_b64 v[70:71], v74
	ds_read_b64 v[72:73], v75
	ds_read_b64 v[74:75], v76
	ds_read_b64 v[76:77], v77
	ds_read_b64 v[78:79], v78
	v_pk_add_f32 v[22:23], v[22:23], v[28:29]
	v_pk_add_f32 v[20:21], v[20:21], v[30:31]
	s_waitcnt lgkmcnt(14)
	v_perm_b32 v28, 0, v32, v169
	v_perm_b32 v29, 0, v32, v170
	v_perm_b32 v30, 0, v33, v169
	v_perm_b32 v31, 0, v33, v170
	v_perm_b32 v32, 0, v34, v169
	v_perm_b32 v33, 0, v34, v170
	v_perm_b32 v34, 0, v35, v169
	v_perm_b32 v35, 0, v35, v170
	v_pk_fma_f16 v28, v88, v28, 0
	v_pk_fma_f16 v29, v88, v29, 0
	v_pk_fma_f16 v30, v88, v30, 0
	v_pk_fma_f16 v31, v88, v31, 0
	s_waitcnt lgkmcnt(13)
	v_perm_b32 v100, 0, v52, v169
	v_perm_b32 v52, 0, v52, v170
	v_perm_b32 v101, 0, v53, v169
	v_perm_b32 v53, 0, v53, v170
	v_pk_fma_f16 v28, v89, v32, v28
	v_pk_fma_f16 v29, v89, v33, v29
	v_pk_fma_f16 v30, v89, v34, v30
	v_pk_fma_f16 v31, v89, v35, v31
	s_waitcnt lgkmcnt(12)
	v_perm_b32 v102, 0, v54, v169
	v_perm_b32 v54, 0, v54, v170
	v_perm_b32 v103, 0, v55, v169
	v_perm_b32 v55, 0, v55, v170
	v_pk_fma_f16 v28, v90, v100, v28
	v_pk_fma_f16 v29, v90, v52, v29
	v_pk_fma_f16 v30, v90, v101, v30
	v_pk_fma_f16 v31, v90, v53, v31
	s_waitcnt lgkmcnt(11)
	v_perm_b32 v104, 0, v56, v169
	v_perm_b32 v56, 0, v56, v170
	v_perm_b32 v105, 0, v57, v169
	v_perm_b32 v57, 0, v57, v170
	v_pk_fma_f16 v28, v91, v102, v28
	v_pk_fma_f16 v29, v91, v54, v29
	v_pk_fma_f16 v30, v91, v103, v30
	v_pk_fma_f16 v31, v91, v55, v31
	s_waitcnt lgkmcnt(10)
	v_perm_b32 v106, 0, v58, v169
	v_perm_b32 v58, 0, v58, v170
	v_perm_b32 v107, 0, v59, v169
	v_perm_b32 v59, 0, v59, v170
	v_pk_fma_f16 v28, v92, v104, v28
	v_pk_fma_f16 v29, v92, v56, v29
	v_pk_fma_f16 v30, v92, v105, v30
	v_pk_fma_f16 v31, v92, v57, v31
	s_waitcnt lgkmcnt(9)
	v_perm_b32 v108, 0, v60, v169
	v_perm_b32 v60, 0, v60, v170
	v_perm_b32 v109, 0, v61, v169
	v_perm_b32 v61, 0, v61, v170
	v_pk_fma_f16 v28, v93, v106, v28
	v_pk_fma_f16 v29, v93, v58, v29
	v_pk_fma_f16 v30, v93, v107, v30
	v_pk_fma_f16 v31, v93, v59, v31
	s_waitcnt lgkmcnt(8)
	v_perm_b32 v110, 0, v62, v169
	v_perm_b32 v62, 0, v62, v170
	v_perm_b32 v111, 0, v63, v169
	v_perm_b32 v63, 0, v63, v170
	v_pk_fma_f16 v28, v94, v108, v28
	v_pk_fma_f16 v29, v94, v60, v29
	v_pk_fma_f16 v30, v94, v109, v30
	v_pk_fma_f16 v31, v94, v61, v31
	s_waitcnt lgkmcnt(7)
; #define VL_LOAD(wr, C) do { _Pragma("unroll") for (int i = 0; i < 16; ++i) wr[i] = wp[(size_t)((C) * 16 + i) * MROWS]; } while (0)
; #define VL_LOAD(wr, C) do { _Pragma("unroll") for (int i = 0; i < 16; ++i) wr[i] = wp[(size_t)((C) * 16 + i) * MROWS]; } while (0)
; template <bool RUN_L = true, bool RUN_G = true, bool DRY = false>
; __device__ __forceinline__ void phase_vaccH(unsigned char* ws, LAS unsigned char* lds, int layer, int G) {
;     ...
; #pragma unroll 1
;             for (int tb = wid; tb < NTB; tb += 4) {
;                 const int tok = tb * 64 + lane; const bool valid = tok < MROWS; const int tokc = valid ? tok : MROWS - 1;
;                 const unsigned* wp = WLT + tokc;
;                 f32x4* hp = (f32x4*)(H + (size_t)tokc * D + cg * 8); const f32x4 h0 = hp[0], h1 = hp[1];
;                 float accf[8];
; #pragma unroll
;                 for (int j = 0; j < 8; ++j) accf[j] = 0.f;
;                 unsigned wa[16], wb[16];
;                 VL_LOAD(wa, 0);
; #pragma unroll 1
;                 for (int c = 0; c < 8; c += 2) {
;                     VL_LOAD(wb, c + 1);
;                     __builtin_amdgcn_sched_barrier(0);
;                     VL_CHUNK(wa);
;                     __builtin_amdgcn_sched_barrier(0);
;                     VL_LOAD(wa, (c + 2) & 7);
;                     __builtin_amdgcn_sched_barrier(0);
;                     VL_CHUNK(wb);
;                     __builtin_amdgcn_sched_barrier(0);
;                 }
;                 if (valid) { hp[0] = h0 + (f32x4){accf[0], accf[1], accf[2], accf[3]}; hp[1] = h1 + (f32x4){accf[4], accf[5], accf[6], accf[7]}; }
	v_perm_b32 v112, 0, v64, v169
	v_perm_b32 v64, 0, v64, v170
	v_perm_b32 v113, 0, v65, v169
	v_perm_b32 v65, 0, v65, v170
	v_pk_fma_f16 v28, v95, v110, v28
	v_pk_fma_f16 v29, v95, v62, v29
	v_pk_fma_f16 v30, v95, v111, v30
	v_pk_fma_f16 v31, v95, v63, v31
	v_perm_b32 v97, v81, v81, s53
	s_waitcnt lgkmcnt(6)
	v_perm_b32 v114, 0, v66, v169
	v_perm_b32 v66, 0, v66, v170
	v_perm_b32 v115, 0, v67, v169
	v_perm_b32 v67, 0, v67, v170
	v_pk_fma_f16 v28, v96, v112, v28
	v_pk_fma_f16 v29, v96, v64, v29
	v_pk_fma_f16 v30, v96, v113, v30
	v_pk_fma_f16 v31, v96, v65, v31
	v_perm_b32 v98, v82, v82, s53
	s_waitcnt lgkmcnt(5)
	v_perm_b32 v116, 0, v68, v169
	v_perm_b32 v68, 0, v68, v170
	v_perm_b32 v117, 0, v69, v169
	v_perm_b32 v69, 0, v69, v170
	v_pk_fma_f16 v28, v97, v114, v28
	v_pk_fma_f16 v29, v97, v66, v29
	v_pk_fma_f16 v30, v97, v115, v30
	v_pk_fma_f16 v31, v97, v67, v31
	v_perm_b32 v99, v83, v83, s53
	s_waitcnt lgkmcnt(4)
	v_perm_b32 v118, 0, v70, v169
	v_perm_b32 v70, 0, v70, v170
	v_perm_b32 v119, 0, v71, v169
	v_perm_b32 v71, 0, v71, v170
	v_pk_fma_f16 v28, v98, v116, v28
	v_pk_fma_f16 v29, v98, v68, v29
	v_pk_fma_f16 v30, v98, v117, v30
	v_pk_fma_f16 v31, v98, v69, v31
	v_perm_b32 v84, v84, v84, s53
	s_waitcnt lgkmcnt(3)
	v_perm_b32 v120, 0, v72, v169
	v_perm_b32 v72, 0, v72, v170
	v_perm_b32 v121, 0, v73, v169
	v_perm_b32 v73, 0, v73, v170
	v_pk_fma_f16 v28, v99, v118, v28
	v_pk_fma_f16 v29, v99, v70, v29
	v_pk_fma_f16 v30, v99, v119, v30
	v_pk_fma_f16 v31, v99, v71, v31
	v_perm_b32 v85, v85, v85, s53
	s_waitcnt lgkmcnt(2)
	v_perm_b32 v122, 0, v74, v169
	v_perm_b32 v74, 0, v74, v170
	v_perm_b32 v123, 0, v75, v169
	v_perm_b32 v75, 0, v75, v170
	v_pk_fma_f16 v28, v84, v120, v28
	v_pk_fma_f16 v29, v84, v72, v29
	v_pk_fma_f16 v30, v84, v121, v30
	v_pk_fma_f16 v31, v84, v73, v31
	v_perm_b32 v86, v86, v86, s53
	s_waitcnt lgkmcnt(1)
	v_perm_b32 v124, 0, v76, v169
	v_perm_b32 v76, 0, v76, v170
	v_perm_b32 v125, 0, v77, v169
	v_perm_b32 v77, 0, v77, v170
	v_pk_fma_f16 v28, v85, v122, v28
	v_pk_fma_f16 v29, v85, v74, v29
	v_pk_fma_f16 v30, v85, v123, v30
	v_pk_fma_f16 v31, v85, v75, v31
	v_perm_b32 v87, v87, v87, s53
	s_waitcnt lgkmcnt(0)
	v_perm_b32 v126, 0, v78, v169
	v_perm_b32 v78, 0, v78, v170
	v_perm_b32 v127, 0, v79, v169
	v_perm_b32 v79, 0, v79, v170
	v_pk_fma_f16 v28, v86, v124, v28
	v_pk_fma_f16 v29, v86, v76, v29
	v_pk_fma_f16 v30, v86, v125, v30
	v_pk_fma_f16 v31, v86, v77, v31
	v_pk_fma_f16 v35, v87, v126, v28
	v_pk_fma_f16 v33, v87, v78, v29
	v_pk_fma_f16 v29, v87, v127, v30
	v_pk_fma_f16 v31, v87, v79, v31
	v_cvt_f32_f16_e32 v34, v35
	v_cvt_f32_f16_e32 v32, v33
	v_cvt_f32_f16_e32 v28, v29
	v_cvt_f32_f16_e32 v30, v31
	v_cvt_f32_f16_sdwa v31, v31 dst_sel:DWORD dst_unused:UNUSED_PAD src0_sel:WORD_1
	v_cvt_f32_f16_sdwa v29, v29 dst_sel:DWORD dst_unused:UNUSED_PAD src0_sel:WORD_1
	v_cvt_f32_f16_sdwa v33, v33 dst_sel:DWORD dst_unused:UNUSED_PAD src0_sel:WORD_1
	v_cvt_f32_f16_sdwa v35, v35 dst_sel:DWORD dst_unused:UNUSED_PAD src0_sel:WORD_1
	v_pk_add_f32 v[80:81], v[18:19], v[24:25]
	v_pk_add_f32 v[82:83], v[16:17], v[26:27]
	v_pk_add_f32 v[20:21], v[20:21], v[30:31]
	v_pk_add_f32 v[22:23], v[22:23], v[28:29]
	v_pk_add_f32 v[30:31], v[82:83], v[32:33]
	v_pk_add_f32 v[28:29], v[80:81], v[34:35]
	s_add_u32 s76, s76, s20
	s_addc_u32 s77, s77, s21
	s_add_i32 s30, s30, 32
	s_add_i32 s31, s31, 2
	s_cmp_lt_u32 s31, 6
	v_lshl_add_u64 v[14:15], v[14:15], 0, s[20:21]
	s_cbranch_scc1 .LBB0_1987
	s_and_saveexec_b64 s[30:31], s[6:7]
	v_pk_add_f32 v[12:13], v[18:19], v[24:25]
	v_pk_add_f32 v[14:15], v[16:17], v[26:27]
	v_pk_add_f32 v[12:13], v[12:13], v[34:35]
	v_pk_add_f32 v[14:15], v[14:15], v[32:33]
	v_pk_add_f32 v[6:7], v[6:7], v[12:13]
	v_pk_add_f32 v[8:9], v[8:9], v[14:15]
	v_pk_add_f32 v[4:5], v[4:5], v[20:21]
	v_pk_add_f32 v[2:3], v[2:3], v[22:23]
	global_store_dwordx4 v[10:11], v[6:9], off
	global_store_dwordx4 v[10:11], v[2:5], off offset:16
	s_branch .LBB0_1985
